# baseline (speedup 1.0000x reference)
.Lh_no_out:
	s_cmp_eq_u32 s17, 0
	s_cselect_b32 s4, s4, s6
	s_cselect_b32 s5, s5, s7
	s_add_u32 s24, s8, s22
	s_addc_u32 s25, s9, 0
	s_add_u32 s4, s4, s21
	s_addc_u32 s5, s5, 0
	s_cmp_lg_u32 s17, 0
	s_cbranch_scc1 .Lh_skip_mask
	global_load_dwordx4 v[14:17], v18, s[24:25] nt
.Lh_skip_mask:
	global_load_dwordx4 v[2:5], v18, s[4:5] nt
	s_add_u32 s6, s4, 0x40000
	s_addc_u32 s7, s5, 0
	s_add_u32 s8, s4, 0x80000
	s_addc_u32 s9, s5, 0
	s_barrier
	global_load_dwordx4 v[6:9], v18, s[6:7] nt
	s_mul_i32 s46, s3, 0xc00
	s_add_u32 s46, s46, 0x8420
	v_lshl_add_u32 v26, v1, 2, s46
	v_and_b32_e32 v38, 15, v0
	s_mul_i32 s58, s17, 0x4200
	s_add_u32 s58, s58, 0x1e0
	v_lshl_add_u32 v38, v38, 2, s58
	v_add_u32_e32 v39, 0x1600, v38
	v_add_u32_e32 v40, 0x2c00, v38
	v_mov_b32_e32 v41, 0x41fc0000
	v_mov_b32_e32 v42, 0xbf38aa3b
	s_mov_b32 s48, 0x3f940000
	s_mov_b32 s51, 0x3fb8aa3b
	s_mov_b32 s42, 0
	s_mov_b32 s43, 0
	s_mov_b32 s44, 0x7fffffff
	s_mov_b32 s45, 0x7fffffff
	s_mov_b32 s47, 0
	s_mul_i32 s58, s3, 0x1600
	s_add_u32 s58, s58, 0x320
	v_lshl_add_u32 v44, v1, 6, s58
	v_bfe_u32 v45, v1, 2, 2
	v_lshlrev_b32_e32 v45, 4, v45
	v_xor_b32_e32 v46, 16, v45
	v_xor_b32_e32 v47, 32, v45
	v_xor_b32_e32 v48, 48, v45
	v_add_u32_e32 v45, v44, v45
	v_add_u32_e32 v46, v44, v46
	v_add_u32_e32 v47, v44, v47
	v_add_u32_e32 v48, v44, v48
	s_mul_i32 s58, s2, 0x600
	s_lshl_b32 s59, s3, 8
	s_add_u32 s58, s58, s59
	s_add_u32 s10, s10, s58
	s_addc_u32 s11, s11, 0
	v_lshlrev_b32_e32 v49, 2, v1
	s_lshl_b32 s58, s2, 2
	s_add_u32 s12, s12, s58
	s_addc_u32 s13, s13, 0
	s_lshl_b32 s58, s16, 5
	s_add_u32 s58, s58, 0x14420
	v_mov_b32_e32 v36, s58
	s_cmp_lg_u32 s17, 0
	s_cbranch_scc1 .Lh_mask_wait
	s_waitcnt vmcnt(2)
	v_cmp_lt_f32_e64 s[26:27], 0.5, v14
	v_cmp_lt_f32_e64 s[28:29], 0.5, v15
	v_cmp_lt_f32_e64 s[30:31], 0.5, v16
	v_cmp_lt_f32_e64 s[32:33], 0.5, v17
	s_bcnt1_i32_b64 s54, s[26:27]
	s_bcnt1_i32_b64 s55, s[28:29]
	s_bcnt1_i32_b64 s56, s[30:31]
	s_bcnt1_i32_b64 s57, s[32:33]
	s_add_i32 s54, s54, s55
	s_add_i32 s56, s56, s57
	s_add_i32 s54, s54, s56
	s_lshl_b32 s55, s16, 2
	v_mov_b32_e32 v37, s55
	v_mov_b32_e32 v27, s54
	v_mov_b32_e32 v28, s26
	v_mov_b32_e32 v29, s27
	v_mov_b32_e32 v30, s28
	v_mov_b32_e32 v31, s29
	v_mov_b32_e32 v32, s30
	v_mov_b32_e32 v33, s31
	v_mov_b32_e32 v34, s32
	v_mov_b32_e32 v35, s33
	s_mov_b64 exec, 1
	ds_write_b32 v37, v27
	ds_write_b128 v36, v[28:31]
	ds_write_b128 v36, v[32:35] offset:16
	s_mov_b64 exec, -1
	s_waitcnt lgkmcnt(0)
.Lh_mask_wait:
	s_barrier
	global_load_dwordx4 v[10:13], v18, s[8:9] nt
	s_cmp_eq_u32 s17, 0
	s_cbranch_scc1 .Lh_have_mask
	ds_read_b128 v[28:31], v36
	ds_read_b128 v[32:35], v36 offset:16
	s_waitcnt lgkmcnt(0)
	v_readfirstlane_b32 s26, v28
	v_readfirstlane_b32 s27, v29
	v_readfirstlane_b32 s28, v30
	v_readfirstlane_b32 s29, v31
	v_readfirstlane_b32 s30, v32
	v_readfirstlane_b32 s31, v33
	v_readfirstlane_b32 s32, v34
	v_readfirstlane_b32 s33, v35
.Lh_have_mask:
	s_setprio 3
	s_cmp_lt_u32 s3, 8
	s_cbranch_scc1 .Lh_nostagger
	s_sleep 3
